# baseline (speedup 1.0000x reference)
.Lk_first:
	ds_read_b128 v[130:133], v219 offset:32768
	ds_read_b128 v[134:137], v219 offset:33792
	ds_read_b128 v[138:141], v219 offset:34816
	ds_read_b128 v[142:145], v219 offset:35840
	ds_read_b128 v[178:181], v219 offset:49152
	ds_read_b128 v[182:185], v219 offset:50176
	ds_read_b128 v[186:189], v219 offset:51200
	ds_read_b128 v[190:193], v219 offset:52224
	ds_read_b128 v[146:149], v220
	ds_read_b128 v[150:153], v220 offset:1024
	ds_read_b128 v[154:157], v221
	ds_read_b128 v[158:161], v221 offset:1024
	ds_read_b128 v[162:165], v222
	ds_read_b128 v[166:169], v222 offset:1024
	ds_read_b128 v[170:173], v223
	ds_read_b128 v[174:177], v223 offset:1024
	s_add_i32 s12, s8, 1
	s_mov_b32 m0, s43
	v_readlane_b32 s9, v248, s12
	s_nop 1
	v_add_u32_e32 v251, s9, v249
	global_load_lds_dwordx4 v251, s[18:19]
	v_add_u32_e32 v251, s9, v250
	s_mov_b32 m0, s44
	s_nop 0
	global_load_lds_dwordx4 v251, s[18:19]
	s_waitcnt lgkmcnt(0)
	s_barrier
	s_setprio 1
	v_mfma_f32_16x16x32_f16 v[124:127], v[130:133], v[146:149], 0
	v_mfma_f32_16x16x32_f16 v[120:123], v[138:141], v[146:149], 0
	v_mfma_f32_16x16x32_f16 v[116:119], v[130:133], v[154:157], 0
	v_mfma_f32_16x16x32_f16 v[112:115], v[138:141], v[154:157], 0
	v_mfma_f32_16x16x32_f16 v[108:111], v[130:133], v[162:165], 0
	v_mfma_f32_16x16x32_f16 v[104:107], v[138:141], v[162:165], 0
	v_mfma_f32_16x16x32_f16 v[100:103], v[130:133], v[170:173], 0
	v_mfma_f32_16x16x32_f16 v[96:99], v[138:141], v[170:173], 0
	v_mfma_f32_16x16x32_f16 v[124:127], v[134:137], v[150:153], v[124:127]
	v_mfma_f32_16x16x32_f16 v[120:123], v[142:145], v[150:153], v[120:123]
	v_mfma_f32_16x16x32_f16 v[116:119], v[134:137], v[158:161], v[116:119]
	v_mfma_f32_16x16x32_f16 v[112:115], v[142:145], v[158:161], v[112:115]
	v_mfma_f32_16x16x32_f16 v[108:111], v[134:137], v[166:169], v[108:111]
	v_mfma_f32_16x16x32_f16 v[104:107], v[142:145], v[166:169], v[104:107]
	v_mfma_f32_16x16x32_f16 v[100:103], v[134:137], v[174:177], v[100:103]
	v_mfma_f32_16x16x32_f16 v[96:99], v[142:145], v[174:177], v[96:99]
	v_mfma_f32_16x16x32_f16 v[52:55], v[178:181], v[146:149], 0
	v_mfma_f32_16x16x32_f16 v[40:43], v[186:189], v[146:149], 0
	v_mfma_f32_16x16x32_f16 v[36:39], v[178:181], v[154:157], 0
	v_mfma_f32_16x16x32_f16 v[32:35], v[186:189], v[154:157], 0
	v_mfma_f32_16x16x32_f16 v[28:31], v[178:181], v[162:165], 0
	v_mfma_f32_16x16x32_f16 v[24:27], v[186:189], v[162:165], 0
	v_mfma_f32_16x16x32_f16 v[20:23], v[178:181], v[170:173], 0
	v_mfma_f32_16x16x32_f16 v[16:19], v[186:189], v[170:173], 0
	v_mfma_f32_16x16x32_f16 v[52:55], v[182:185], v[150:153], v[52:55]
	v_mfma_f32_16x16x32_f16 v[40:43], v[190:193], v[150:153], v[40:43]
	v_mfma_f32_16x16x32_f16 v[36:39], v[182:185], v[158:161], v[36:39]
	v_mfma_f32_16x16x32_f16 v[32:35], v[190:193], v[158:161], v[32:35]
	v_mfma_f32_16x16x32_f16 v[28:31], v[182:185], v[166:169], v[28:31]
	v_mfma_f32_16x16x32_f16 v[24:27], v[190:193], v[166:169], v[24:27]
	v_mfma_f32_16x16x32_f16 v[20:23], v[182:185], v[174:177], v[20:23]
	v_mfma_f32_16x16x32_f16 v[16:19], v[190:193], v[174:177], v[16:19]
	s_setprio 0
	s_barrier
	ds_read_b128 v[146:149], v220 offset:16384
	ds_read_b128 v[150:153], v220 offset:17408
	ds_read_b128 v[154:157], v221 offset:16384
	ds_read_b128 v[158:161], v221 offset:17408
	ds_read_b128 v[162:165], v222 offset:16384
	ds_read_b128 v[166:169], v222 offset:17408
	ds_read_b128 v[170:173], v223 offset:16384
	ds_read_b128 v[174:177], v223 offset:17408
	v_add_u32_e32 v129, s7, v128
	s_mov_b32 m0, s22
	v_add_u32_e32 v194, 0xffffff80, v129
	global_load_lds_dwordx4 v194, s[10:11]
	v_add_u32_e32 v194, 0x47f80, v129
	s_mov_b32 m0, s23
	s_add_i32 s9, s8, 2
	global_load_lds_dwordx4 v194, s[10:11]
	v_readlane_b32 s13, v248, s9
	s_mov_b32 m0, s21
	s_nop 1
	v_add_u32_e32 v194, s13, v206
	global_load_lds_dwordx4 v194, s[18:19]
	v_add_u32_e32 v194, s13, v213
	s_mov_b32 m0, s24
	s_nop 0
	global_load_lds_dwordx4 v194, s[18:19]
	s_mov_b32 m0, s25
	v_add_u32_e32 v194, 0x8ff80, v129
	global_load_lds_dwordx4 v194, s[10:11]
	v_add_u32_e32 v194, 0xd7f80, v129
	s_mov_b32 m0, s26
	s_nop 0
	global_load_lds_dwordx4 v194, s[10:11]
	s_waitcnt vmcnt(8) lgkmcnt(0)
	s_barrier
	s_setprio 1
	v_mfma_f32_16x16x32_f16 v[12:15], v[130:133], v[146:149], 0
	v_mfma_f32_16x16x32_f16 v[8:11], v[138:141], v[146:149], 0
	v_mfma_f32_16x16x32_f16 v[4:7], v[130:133], v[154:157], 0
	v_mfma_f32_16x16x32_f16 v[0:3], v[138:141], v[154:157], 0
	v_mfma_f32_16x16x32_f16 v[44:47], v[130:133], v[162:165], 0
	v_mfma_f32_16x16x32_f16 v[48:51], v[138:141], v[162:165], 0
	v_mfma_f32_16x16x32_f16 v[56:59], v[130:133], v[170:173], 0
	v_mfma_f32_16x16x32_f16 v[60:63], v[138:141], v[170:173], 0
	v_mfma_f32_16x16x32_f16 v[12:15], v[134:137], v[150:153], v[12:15]
	v_mfma_f32_16x16x32_f16 v[8:11], v[142:145], v[150:153], v[8:11]
	v_mfma_f32_16x16x32_f16 v[4:7], v[134:137], v[158:161], v[4:7]
	v_mfma_f32_16x16x32_f16 v[0:3], v[142:145], v[158:161], v[0:3]
	v_mfma_f32_16x16x32_f16 v[44:47], v[134:137], v[166:169], v[44:47]
	v_mfma_f32_16x16x32_f16 v[48:51], v[142:145], v[166:169], v[48:51]
	v_mfma_f32_16x16x32_f16 v[56:59], v[134:137], v[174:177], v[56:59]
	v_mfma_f32_16x16x32_f16 v[60:63], v[142:145], v[174:177], v[60:63]
	v_mfma_f32_16x16x32_f16 v[64:67], v[178:181], v[146:149], 0
	v_mfma_f32_16x16x32_f16 v[68:71], v[186:189], v[146:149], 0
	v_mfma_f32_16x16x32_f16 v[72:75], v[178:181], v[154:157], 0
	v_mfma_f32_16x16x32_f16 v[76:79], v[186:189], v[154:157], 0
	v_mfma_f32_16x16x32_f16 v[80:83], v[178:181], v[162:165], 0
	v_mfma_f32_16x16x32_f16 v[84:87], v[186:189], v[162:165], 0
	v_mfma_f32_16x16x32_f16 v[88:91], v[178:181], v[170:173], 0
	v_mfma_f32_16x16x32_f16 v[92:95], v[186:189], v[170:173], 0
	v_mfma_f32_16x16x32_f16 v[64:67], v[182:185], v[150:153], v[64:67]
	v_mfma_f32_16x16x32_f16 v[68:71], v[190:193], v[150:153], v[68:71]
	v_mfma_f32_16x16x32_f16 v[72:75], v[182:185], v[158:161], v[72:75]
	v_mfma_f32_16x16x32_f16 v[76:79], v[190:193], v[158:161], v[76:79]
	v_mfma_f32_16x16x32_f16 v[80:83], v[182:185], v[166:169], v[80:83]
	v_mfma_f32_16x16x32_f16 v[84:87], v[190:193], v[166:169], v[84:87]
	v_mfma_f32_16x16x32_f16 v[88:91], v[182:185], v[174:177], v[88:91]
	v_mfma_f32_16x16x32_f16 v[92:95], v[190:193], v[174:177], v[92:95]
	s_setprio 0
	s_barrier
	ds_read_b128 v[130:133], v224
	ds_read_b128 v[134:137], v224 offset:1024
	ds_read_b128 v[138:141], v224 offset:2048
	ds_read_b128 v[142:145], v224 offset:3072
	ds_read_b128 v[178:181], v229
	ds_read_b128 v[182:185], v229 offset:1024
	ds_read_b128 v[186:189], v229 offset:2048
	ds_read_b128 v[190:193], v229 offset:3072
	ds_read_b128 v[146:149], v225
	ds_read_b128 v[150:153], v225 offset:1024
	ds_read_b128 v[154:157], v226
	ds_read_b128 v[158:161], v226 offset:1024
	ds_read_b128 v[162:165], v227
	ds_read_b128 v[166:169], v227 offset:1024
	ds_read_b128 v[170:173], v228
	ds_read_b128 v[174:177], v228 offset:1024
	v_readlane_b32 s12, v248, s9
	s_mov_b32 m0, s27
	s_nop 1
	v_add_u32_e32 v251, s12, v249
	global_load_lds_dwordx4 v251, s[18:19]
	v_add_u32_e32 v251, s12, v250
	s_mov_b32 m0, s28
	s_nop 0
	global_load_lds_dwordx4 v251, s[18:19]
	s_waitcnt vmcnt(8) lgkmcnt(0)
	s_barrier
	s_setprio 1
	v_mfma_f32_16x16x32_f16 v[124:127], v[130:133], v[146:149], v[124:127]
	v_mfma_f32_16x16x32_f16 v[120:123], v[138:141], v[146:149], v[120:123]
	v_mfma_f32_16x16x32_f16 v[116:119], v[130:133], v[154:157], v[116:119]
	v_mfma_f32_16x16x32_f16 v[112:115], v[138:141], v[154:157], v[112:115]
	v_mfma_f32_16x16x32_f16 v[108:111], v[130:133], v[162:165], v[108:111]
	v_mfma_f32_16x16x32_f16 v[104:107], v[138:141], v[162:165], v[104:107]
	v_mfma_f32_16x16x32_f16 v[100:103], v[130:133], v[170:173], v[100:103]
	v_mfma_f32_16x16x32_f16 v[96:99], v[138:141], v[170:173], v[96:99]
	v_mfma_f32_16x16x32_f16 v[124:127], v[134:137], v[150:153], v[124:127]
	v_mfma_f32_16x16x32_f16 v[120:123], v[142:145], v[150:153], v[120:123]
	v_mfma_f32_16x16x32_f16 v[116:119], v[134:137], v[158:161], v[116:119]
	v_mfma_f32_16x16x32_f16 v[112:115], v[142:145], v[158:161], v[112:115]
	v_mfma_f32_16x16x32_f16 v[108:111], v[134:137], v[166:169], v[108:111]
	v_mfma_f32_16x16x32_f16 v[104:107], v[142:145], v[166:169], v[104:107]
	v_mfma_f32_16x16x32_f16 v[100:103], v[134:137], v[174:177], v[100:103]
	v_mfma_f32_16x16x32_f16 v[96:99], v[142:145], v[174:177], v[96:99]
	v_mfma_f32_16x16x32_f16 v[52:55], v[178:181], v[146:149], v[52:55]
	v_mfma_f32_16x16x32_f16 v[40:43], v[186:189], v[146:149], v[40:43]
	v_mfma_f32_16x16x32_f16 v[36:39], v[178:181], v[154:157], v[36:39]
	v_mfma_f32_16x16x32_f16 v[32:35], v[186:189], v[154:157], v[32:35]
	v_mfma_f32_16x16x32_f16 v[28:31], v[178:181], v[162:165], v[28:31]
	v_mfma_f32_16x16x32_f16 v[24:27], v[186:189], v[162:165], v[24:27]
	v_mfma_f32_16x16x32_f16 v[20:23], v[178:181], v[170:173], v[20:23]
	v_mfma_f32_16x16x32_f16 v[16:19], v[186:189], v[170:173], v[16:19]
	v_mfma_f32_16x16x32_f16 v[52:55], v[182:185], v[150:153], v[52:55]
	v_mfma_f32_16x16x32_f16 v[40:43], v[190:193], v[150:153], v[40:43]
	v_mfma_f32_16x16x32_f16 v[36:39], v[182:185], v[158:161], v[36:39]
	v_mfma_f32_16x16x32_f16 v[32:35], v[190:193], v[158:161], v[32:35]
	v_mfma_f32_16x16x32_f16 v[28:31], v[182:185], v[166:169], v[28:31]
	v_mfma_f32_16x16x32_f16 v[24:27], v[190:193], v[166:169], v[24:27]
	v_mfma_f32_16x16x32_f16 v[20:23], v[182:185], v[174:177], v[20:23]
	v_mfma_f32_16x16x32_f16 v[16:19], v[190:193], v[174:177], v[16:19]
	s_setprio 0
	s_barrier
	ds_read_b128 v[146:149], v230
	ds_read_b128 v[150:153], v230 offset:1024
	ds_read_b128 v[154:157], v231
	ds_read_b128 v[158:161], v231 offset:1024
	ds_read_b128 v[162:165], v232
	ds_read_b128 v[166:169], v232 offset:1024
	ds_read_b128 v[170:173], v233
	ds_read_b128 v[174:177], v233 offset:1024
	s_mov_b32 m0, s37
	v_add_u32_e32 v194, 0x48000, v129
	global_load_lds_dwordx4 v129, s[10:11]
	s_mov_b32 m0, s38
	s_add_i32 s12, s8, 3
	global_load_lds_dwordx4 v194, s[10:11]
	v_readlane_b32 s13, v248, s12
	s_mov_b32 m0, s39
	s_nop 1
	v_add_u32_e32 v194, s13, v206
	global_load_lds_dwordx4 v194, s[18:19]
	v_add_u32_e32 v194, s13, v213
	s_mov_b32 m0, s40
	s_nop 0
	global_load_lds_dwordx4 v194, s[18:19]
	s_mov_b32 m0, s41
	v_add_u32_e32 v194, 0x90000, v129
	global_load_lds_dwordx4 v194, s[10:11]
	v_add_u32_e32 v194, 0xd8000, v129
	s_mov_b32 m0, s42
	s_nop 0
	global_load_lds_dwordx4 v194, s[10:11]
	s_waitcnt vmcnt(8) lgkmcnt(0)
	s_barrier
	s_setprio 1
	v_mfma_f32_16x16x32_f16 v[12:15], v[130:133], v[146:149], v[12:15]
	v_mfma_f32_16x16x32_f16 v[8:11], v[138:141], v[146:149], v[8:11]
	v_mfma_f32_16x16x32_f16 v[4:7], v[130:133], v[154:157], v[4:7]
	v_mfma_f32_16x16x32_f16 v[0:3], v[138:141], v[154:157], v[0:3]
	v_mfma_f32_16x16x32_f16 v[44:47], v[130:133], v[162:165], v[44:47]
	v_mfma_f32_16x16x32_f16 v[48:51], v[138:141], v[162:165], v[48:51]
	v_mfma_f32_16x16x32_f16 v[56:59], v[130:133], v[170:173], v[56:59]
	v_mfma_f32_16x16x32_f16 v[60:63], v[138:141], v[170:173], v[60:63]
	v_mfma_f32_16x16x32_f16 v[12:15], v[134:137], v[150:153], v[12:15]
	v_mfma_f32_16x16x32_f16 v[8:11], v[142:145], v[150:153], v[8:11]
	v_mfma_f32_16x16x32_f16 v[4:7], v[134:137], v[158:161], v[4:7]
	v_mfma_f32_16x16x32_f16 v[0:3], v[142:145], v[158:161], v[0:3]
	v_mfma_f32_16x16x32_f16 v[44:47], v[134:137], v[166:169], v[44:47]
	v_mfma_f32_16x16x32_f16 v[48:51], v[142:145], v[166:169], v[48:51]
	v_mfma_f32_16x16x32_f16 v[56:59], v[134:137], v[174:177], v[56:59]
	v_mfma_f32_16x16x32_f16 v[60:63], v[142:145], v[174:177], v[60:63]
	v_mfma_f32_16x16x32_f16 v[64:67], v[178:181], v[146:149], v[64:67]
	v_mfma_f32_16x16x32_f16 v[68:71], v[186:189], v[146:149], v[68:71]
	v_mfma_f32_16x16x32_f16 v[72:75], v[178:181], v[154:157], v[72:75]
	v_mfma_f32_16x16x32_f16 v[76:79], v[186:189], v[154:157], v[76:79]
	v_mfma_f32_16x16x32_f16 v[80:83], v[178:181], v[162:165], v[80:83]
	v_mfma_f32_16x16x32_f16 v[84:87], v[186:189], v[162:165], v[84:87]
	v_mfma_f32_16x16x32_f16 v[88:91], v[178:181], v[170:173], v[88:91]
	v_mfma_f32_16x16x32_f16 v[92:95], v[186:189], v[170:173], v[92:95]
	v_mfma_f32_16x16x32_f16 v[64:67], v[182:185], v[150:153], v[64:67]
	v_mfma_f32_16x16x32_f16 v[68:71], v[190:193], v[150:153], v[68:71]
	v_mfma_f32_16x16x32_f16 v[72:75], v[182:185], v[158:161], v[72:75]
	v_mfma_f32_16x16x32_f16 v[76:79], v[190:193], v[158:161], v[76:79]
	v_mfma_f32_16x16x32_f16 v[80:83], v[182:185], v[166:169], v[80:83]
	v_mfma_f32_16x16x32_f16 v[84:87], v[190:193], v[166:169], v[84:87]
	v_mfma_f32_16x16x32_f16 v[88:91], v[182:185], v[174:177], v[88:91]
	v_mfma_f32_16x16x32_f16 v[92:95], v[190:193], v[174:177], v[92:95]
	s_setprio 0
	s_addk_i32 s7, 0x100
	s_cmp_lt_u32 s8, 32
	s_mov_b32 s8, s9
	s_barrier
.LBB1_82:
	ds_read_b128 v[130:133], v219 offset:32768
	ds_read_b128 v[134:137], v219 offset:33792
	ds_read_b128 v[138:141], v219 offset:34816
	ds_read_b128 v[142:145], v219 offset:35840
	ds_read_b128 v[178:181], v219 offset:49152
	ds_read_b128 v[182:185], v219 offset:50176
	ds_read_b128 v[186:189], v219 offset:51200
	ds_read_b128 v[190:193], v219 offset:52224
	ds_read_b128 v[146:149], v220
	ds_read_b128 v[150:153], v220 offset:1024
	ds_read_b128 v[154:157], v221
	ds_read_b128 v[158:161], v221 offset:1024
	ds_read_b128 v[162:165], v222
	ds_read_b128 v[166:169], v222 offset:1024
	ds_read_b128 v[170:173], v223
	ds_read_b128 v[174:177], v223 offset:1024
	s_add_i32 s12, s8, 1
	s_mov_b32 m0, s43
	v_readlane_b32 s9, v248, s12
	s_nop 1
	v_add_u32_e32 v251, s9, v249
	global_load_lds_dwordx4 v251, s[18:19]
	v_add_u32_e32 v251, s9, v250
	s_mov_b32 m0, s44
	s_nop 0
	global_load_lds_dwordx4 v251, s[18:19]
	s_waitcnt vmcnt(8) lgkmcnt(0)
	s_barrier
	s_setprio 1
	v_mfma_f32_16x16x32_f16 v[124:127], v[130:133], v[146:149], v[124:127]
	v_mfma_f32_16x16x32_f16 v[120:123], v[138:141], v[146:149], v[120:123]
	v_mfma_f32_16x16x32_f16 v[116:119], v[130:133], v[154:157], v[116:119]
	v_mfma_f32_16x16x32_f16 v[112:115], v[138:141], v[154:157], v[112:115]
	v_mfma_f32_16x16x32_f16 v[108:111], v[130:133], v[162:165], v[108:111]
	v_mfma_f32_16x16x32_f16 v[104:107], v[138:141], v[162:165], v[104:107]
	v_mfma_f32_16x16x32_f16 v[100:103], v[130:133], v[170:173], v[100:103]
	v_mfma_f32_16x16x32_f16 v[96:99], v[138:141], v[170:173], v[96:99]
	v_mfma_f32_16x16x32_f16 v[124:127], v[134:137], v[150:153], v[124:127]
	v_mfma_f32_16x16x32_f16 v[120:123], v[142:145], v[150:153], v[120:123]
	v_mfma_f32_16x16x32_f16 v[116:119], v[134:137], v[158:161], v[116:119]
	v_mfma_f32_16x16x32_f16 v[112:115], v[142:145], v[158:161], v[112:115]
	v_mfma_f32_16x16x32_f16 v[108:111], v[134:137], v[166:169], v[108:111]
	v_mfma_f32_16x16x32_f16 v[104:107], v[142:145], v[166:169], v[104:107]
	v_mfma_f32_16x16x32_f16 v[100:103], v[134:137], v[174:177], v[100:103]
	v_mfma_f32_16x16x32_f16 v[96:99], v[142:145], v[174:177], v[96:99]
	v_mfma_f32_16x16x32_f16 v[52:55], v[178:181], v[146:149], v[52:55]
	v_mfma_f32_16x16x32_f16 v[40:43], v[186:189], v[146:149], v[40:43]
	v_mfma_f32_16x16x32_f16 v[36:39], v[178:181], v[154:157], v[36:39]
	v_mfma_f32_16x16x32_f16 v[32:35], v[186:189], v[154:157], v[32:35]
	v_mfma_f32_16x16x32_f16 v[28:31], v[178:181], v[162:165], v[28:31]
	v_mfma_f32_16x16x32_f16 v[24:27], v[186:189], v[162:165], v[24:27]
	v_mfma_f32_16x16x32_f16 v[20:23], v[178:181], v[170:173], v[20:23]
	v_mfma_f32_16x16x32_f16 v[16:19], v[186:189], v[170:173], v[16:19]
	v_mfma_f32_16x16x32_f16 v[52:55], v[182:185], v[150:153], v[52:55]
	v_mfma_f32_16x16x32_f16 v[40:43], v[190:193], v[150:153], v[40:43]
	v_mfma_f32_16x16x32_f16 v[36:39], v[182:185], v[158:161], v[36:39]
	v_mfma_f32_16x16x32_f16 v[32:35], v[190:193], v[158:161], v[32:35]
	v_mfma_f32_16x16x32_f16 v[28:31], v[182:185], v[166:169], v[28:31]
	v_mfma_f32_16x16x32_f16 v[24:27], v[190:193], v[166:169], v[24:27]
	v_mfma_f32_16x16x32_f16 v[20:23], v[182:185], v[174:177], v[20:23]
	v_mfma_f32_16x16x32_f16 v[16:19], v[190:193], v[174:177], v[16:19]
	s_setprio 0
	s_barrier
	ds_read_b128 v[146:149], v220 offset:16384
	ds_read_b128 v[150:153], v220 offset:17408
	ds_read_b128 v[154:157], v221 offset:16384
	ds_read_b128 v[158:161], v221 offset:17408
	ds_read_b128 v[162:165], v222 offset:16384
	ds_read_b128 v[166:169], v222 offset:17408
	ds_read_b128 v[170:173], v223 offset:16384
	ds_read_b128 v[174:177], v223 offset:17408
	v_add_u32_e32 v129, s7, v128
	s_mov_b32 m0, s22
	v_add_u32_e32 v194, 0xffffff80, v129
	global_load_lds_dwordx4 v194, s[10:11]
	v_add_u32_e32 v194, 0x47f80, v129
	s_mov_b32 m0, s23
	s_add_i32 s9, s8, 2
	global_load_lds_dwordx4 v194, s[10:11]
	v_readlane_b32 s13, v248, s9
	s_mov_b32 m0, s21
	s_nop 1
	v_add_u32_e32 v194, s13, v206
	global_load_lds_dwordx4 v194, s[18:19]
	v_add_u32_e32 v194, s13, v213
	s_mov_b32 m0, s24
	s_nop 0
	global_load_lds_dwordx4 v194, s[18:19]
	s_mov_b32 m0, s25
	v_add_u32_e32 v194, 0x8ff80, v129
	global_load_lds_dwordx4 v194, s[10:11]
	v_add_u32_e32 v194, 0xd7f80, v129
	s_mov_b32 m0, s26
	s_nop 0
	global_load_lds_dwordx4 v194, s[10:11]
	s_waitcnt vmcnt(8) lgkmcnt(0)
	s_barrier
	s_setprio 1
	v_mfma_f32_16x16x32_f16 v[12:15], v[130:133], v[146:149], v[12:15]
	v_mfma_f32_16x16x32_f16 v[8:11], v[138:141], v[146:149], v[8:11]
	v_mfma_f32_16x16x32_f16 v[4:7], v[130:133], v[154:157], v[4:7]
	v_mfma_f32_16x16x32_f16 v[0:3], v[138:141], v[154:157], v[0:3]
	v_mfma_f32_16x16x32_f16 v[44:47], v[130:133], v[162:165], v[44:47]
	v_mfma_f32_16x16x32_f16 v[48:51], v[138:141], v[162:165], v[48:51]
	v_mfma_f32_16x16x32_f16 v[56:59], v[130:133], v[170:173], v[56:59]
	v_mfma_f32_16x16x32_f16 v[60:63], v[138:141], v[170:173], v[60:63]
	v_mfma_f32_16x16x32_f16 v[12:15], v[134:137], v[150:153], v[12:15]
	v_mfma_f32_16x16x32_f16 v[8:11], v[142:145], v[150:153], v[8:11]
	v_mfma_f32_16x16x32_f16 v[4:7], v[134:137], v[158:161], v[4:7]
	v_mfma_f32_16x16x32_f16 v[0:3], v[142:145], v[158:161], v[0:3]
	v_mfma_f32_16x16x32_f16 v[44:47], v[134:137], v[166:169], v[44:47]
	v_mfma_f32_16x16x32_f16 v[48:51], v[142:145], v[166:169], v[48:51]
	v_mfma_f32_16x16x32_f16 v[56:59], v[134:137], v[174:177], v[56:59]
	v_mfma_f32_16x16x32_f16 v[60:63], v[142:145], v[174:177], v[60:63]
	v_mfma_f32_16x16x32_f16 v[64:67], v[178:181], v[146:149], v[64:67]
	v_mfma_f32_16x16x32_f16 v[68:71], v[186:189], v[146:149], v[68:71]
	v_mfma_f32_16x16x32_f16 v[72:75], v[178:181], v[154:157], v[72:75]
	v_mfma_f32_16x16x32_f16 v[76:79], v[186:189], v[154:157], v[76:79]
	v_mfma_f32_16x16x32_f16 v[80:83], v[178:181], v[162:165], v[80:83]
	v_mfma_f32_16x16x32_f16 v[84:87], v[186:189], v[162:165], v[84:87]
	v_mfma_f32_16x16x32_f16 v[88:91], v[178:181], v[170:173], v[88:91]
	v_mfma_f32_16x16x32_f16 v[92:95], v[186:189], v[170:173], v[92:95]
	v_mfma_f32_16x16x32_f16 v[64:67], v[182:185], v[150:153], v[64:67]
	v_mfma_f32_16x16x32_f16 v[68:71], v[190:193], v[150:153], v[68:71]
	v_mfma_f32_16x16x32_f16 v[72:75], v[182:185], v[158:161], v[72:75]
	v_mfma_f32_16x16x32_f16 v[76:79], v[190:193], v[158:161], v[76:79]
	v_mfma_f32_16x16x32_f16 v[80:83], v[182:185], v[166:169], v[80:83]
	v_mfma_f32_16x16x32_f16 v[84:87], v[190:193], v[166:169], v[84:87]
	v_mfma_f32_16x16x32_f16 v[88:91], v[182:185], v[174:177], v[88:91]
	v_mfma_f32_16x16x32_f16 v[92:95], v[190:193], v[174:177], v[92:95]
	s_setprio 0
	s_barrier
	ds_read_b128 v[130:133], v224
	ds_read_b128 v[134:137], v224 offset:1024
	ds_read_b128 v[138:141], v224 offset:2048
	ds_read_b128 v[142:145], v224 offset:3072
	ds_read_b128 v[178:181], v229
	ds_read_b128 v[182:185], v229 offset:1024
	ds_read_b128 v[186:189], v229 offset:2048
	ds_read_b128 v[190:193], v229 offset:3072
	ds_read_b128 v[146:149], v225
	ds_read_b128 v[150:153], v225 offset:1024
	ds_read_b128 v[154:157], v226
	ds_read_b128 v[158:161], v226 offset:1024
	ds_read_b128 v[162:165], v227
	ds_read_b128 v[166:169], v227 offset:1024
	ds_read_b128 v[170:173], v228
	ds_read_b128 v[174:177], v228 offset:1024
	v_readlane_b32 s12, v248, s9
	s_mov_b32 m0, s27
	s_nop 1
	v_add_u32_e32 v251, s12, v249
	global_load_lds_dwordx4 v251, s[18:19]
	v_add_u32_e32 v251, s12, v250
	s_mov_b32 m0, s28
	s_nop 0
	global_load_lds_dwordx4 v251, s[18:19]
	s_waitcnt vmcnt(8) lgkmcnt(0)
	s_barrier
	s_setprio 1
	v_mfma_f32_16x16x32_f16 v[124:127], v[130:133], v[146:149], v[124:127]
	v_mfma_f32_16x16x32_f16 v[120:123], v[138:141], v[146:149], v[120:123]
	v_mfma_f32_16x16x32_f16 v[116:119], v[130:133], v[154:157], v[116:119]
	v_mfma_f32_16x16x32_f16 v[112:115], v[138:141], v[154:157], v[112:115]
	v_mfma_f32_16x16x32_f16 v[108:111], v[130:133], v[162:165], v[108:111]
	v_mfma_f32_16x16x32_f16 v[104:107], v[138:141], v[162:165], v[104:107]
	v_mfma_f32_16x16x32_f16 v[100:103], v[130:133], v[170:173], v[100:103]
	v_mfma_f32_16x16x32_f16 v[96:99], v[138:141], v[170:173], v[96:99]
	v_mfma_f32_16x16x32_f16 v[124:127], v[134:137], v[150:153], v[124:127]
	v_mfma_f32_16x16x32_f16 v[120:123], v[142:145], v[150:153], v[120:123]
	v_mfma_f32_16x16x32_f16 v[116:119], v[134:137], v[158:161], v[116:119]
	v_mfma_f32_16x16x32_f16 v[112:115], v[142:145], v[158:161], v[112:115]
	v_mfma_f32_16x16x32_f16 v[108:111], v[134:137], v[166:169], v[108:111]
	v_mfma_f32_16x16x32_f16 v[104:107], v[142:145], v[166:169], v[104:107]
	v_mfma_f32_16x16x32_f16 v[100:103], v[134:137], v[174:177], v[100:103]
	v_mfma_f32_16x16x32_f16 v[96:99], v[142:145], v[174:177], v[96:99]
	v_mfma_f32_16x16x32_f16 v[52:55], v[178:181], v[146:149], v[52:55]
	v_mfma_f32_16x16x32_f16 v[40:43], v[186:189], v[146:149], v[40:43]
	v_mfma_f32_16x16x32_f16 v[36:39], v[178:181], v[154:157], v[36:39]
	v_mfma_f32_16x16x32_f16 v[32:35], v[186:189], v[154:157], v[32:35]
	v_mfma_f32_16x16x32_f16 v[28:31], v[178:181], v[162:165], v[28:31]
	v_mfma_f32_16x16x32_f16 v[24:27], v[186:189], v[162:165], v[24:27]
	v_mfma_f32_16x16x32_f16 v[20:23], v[178:181], v[170:173], v[20:23]
	v_mfma_f32_16x16x32_f16 v[16:19], v[186:189], v[170:173], v[16:19]
	v_mfma_f32_16x16x32_f16 v[52:55], v[182:185], v[150:153], v[52:55]
	v_mfma_f32_16x16x32_f16 v[40:43], v[190:193], v[150:153], v[40:43]
	v_mfma_f32_16x16x32_f16 v[36:39], v[182:185], v[158:161], v[36:39]
	v_mfma_f32_16x16x32_f16 v[32:35], v[190:193], v[158:161], v[32:35]
	v_mfma_f32_16x16x32_f16 v[28:31], v[182:185], v[166:169], v[28:31]
	v_mfma_f32_16x16x32_f16 v[24:27], v[190:193], v[166:169], v[24:27]
	v_mfma_f32_16x16x32_f16 v[20:23], v[182:185], v[174:177], v[20:23]
	v_mfma_f32_16x16x32_f16 v[16:19], v[190:193], v[174:177], v[16:19]
	s_setprio 0
	s_barrier
	ds_read_b128 v[146:149], v230
	ds_read_b128 v[150:153], v230 offset:1024
	ds_read_b128 v[154:157], v231
	ds_read_b128 v[158:161], v231 offset:1024
	ds_read_b128 v[162:165], v232
	ds_read_b128 v[166:169], v232 offset:1024
	ds_read_b128 v[170:173], v233
	ds_read_b128 v[174:177], v233 offset:1024
	s_mov_b32 m0, s37
	v_add_u32_e32 v194, 0x48000, v129
	global_load_lds_dwordx4 v129, s[10:11]
	s_mov_b32 m0, s38
	s_add_i32 s12, s8, 3
	global_load_lds_dwordx4 v194, s[10:11]
	v_readlane_b32 s13, v248, s12
	s_mov_b32 m0, s39
	s_nop 1
	v_add_u32_e32 v194, s13, v206
	global_load_lds_dwordx4 v194, s[18:19]
	v_add_u32_e32 v194, s13, v213
	s_mov_b32 m0, s40
	s_nop 0
	global_load_lds_dwordx4 v194, s[18:19]
	s_mov_b32 m0, s41
	v_add_u32_e32 v194, 0x90000, v129
	global_load_lds_dwordx4 v194, s[10:11]
	v_add_u32_e32 v194, 0xd8000, v129
	s_mov_b32 m0, s42
	s_nop 0
	global_load_lds_dwordx4 v194, s[10:11]
	s_waitcnt vmcnt(8) lgkmcnt(0)
	s_barrier
	s_setprio 1
	v_mfma_f32_16x16x32_f16 v[12:15], v[130:133], v[146:149], v[12:15]
	v_mfma_f32_16x16x32_f16 v[8:11], v[138:141], v[146:149], v[8:11]
	v_mfma_f32_16x16x32_f16 v[4:7], v[130:133], v[154:157], v[4:7]
	v_mfma_f32_16x16x32_f16 v[0:3], v[138:141], v[154:157], v[0:3]
	v_mfma_f32_16x16x32_f16 v[44:47], v[130:133], v[162:165], v[44:47]
	v_mfma_f32_16x16x32_f16 v[48:51], v[138:141], v[162:165], v[48:51]
	v_mfma_f32_16x16x32_f16 v[56:59], v[130:133], v[170:173], v[56:59]
	v_mfma_f32_16x16x32_f16 v[60:63], v[138:141], v[170:173], v[60:63]
	v_mfma_f32_16x16x32_f16 v[12:15], v[134:137], v[150:153], v[12:15]
	v_mfma_f32_16x16x32_f16 v[8:11], v[142:145], v[150:153], v[8:11]
	v_mfma_f32_16x16x32_f16 v[4:7], v[134:137], v[158:161], v[4:7]
	v_mfma_f32_16x16x32_f16 v[0:3], v[142:145], v[158:161], v[0:3]
	v_mfma_f32_16x16x32_f16 v[44:47], v[134:137], v[166:169], v[44:47]
	v_mfma_f32_16x16x32_f16 v[48:51], v[142:145], v[166:169], v[48:51]
	v_mfma_f32_16x16x32_f16 v[56:59], v[134:137], v[174:177], v[56:59]
	v_mfma_f32_16x16x32_f16 v[60:63], v[142:145], v[174:177], v[60:63]
	v_mfma_f32_16x16x32_f16 v[64:67], v[178:181], v[146:149], v[64:67]
	v_mfma_f32_16x16x32_f16 v[68:71], v[186:189], v[146:149], v[68:71]
	v_mfma_f32_16x16x32_f16 v[72:75], v[178:181], v[154:157], v[72:75]
	v_mfma_f32_16x16x32_f16 v[76:79], v[186:189], v[154:157], v[76:79]
	v_mfma_f32_16x16x32_f16 v[80:83], v[178:181], v[162:165], v[80:83]
	v_mfma_f32_16x16x32_f16 v[84:87], v[186:189], v[162:165], v[84:87]
	v_mfma_f32_16x16x32_f16 v[88:91], v[178:181], v[170:173], v[88:91]
	v_mfma_f32_16x16x32_f16 v[92:95], v[186:189], v[170:173], v[92:95]
	v_mfma_f32_16x16x32_f16 v[64:67], v[182:185], v[150:153], v[64:67]
	v_mfma_f32_16x16x32_f16 v[68:71], v[190:193], v[150:153], v[68:71]
	v_mfma_f32_16x16x32_f16 v[72:75], v[182:185], v[158:161], v[72:75]
	v_mfma_f32_16x16x32_f16 v[76:79], v[190:193], v[158:161], v[76:79]
	v_mfma_f32_16x16x32_f16 v[80:83], v[182:185], v[166:169], v[80:83]
	v_mfma_f32_16x16x32_f16 v[84:87], v[190:193], v[166:169], v[84:87]
	v_mfma_f32_16x16x32_f16 v[88:91], v[182:185], v[174:177], v[88:91]
	v_mfma_f32_16x16x32_f16 v[92:95], v[190:193], v[174:177], v[92:95]
	s_setprio 0
	s_addk_i32 s7, 0x100
	s_cmp_lt_u32 s8, 32
	s_mov_b32 s8, s9
	s_barrier
	s_cbranch_scc1 .LBB1_82
	ds_read_b128 v[132:135], v219 offset:32768
	ds_read_b128 v[136:139], v219 offset:33792
	ds_read_b128 v[140:143], v219 offset:34816
	ds_read_b128 v[144:147], v219 offset:35840
	ds_read_b128 v[128:131], v220
	ds_read_b128 v[148:151], v220 offset:1024
	ds_read_b128 v[152:155], v221
	ds_read_b128 v[156:159], v221 offset:1024
	ds_read_b128 v[188:191], v222
	ds_read_b128 v[192:195], v222 offset:1024
	ds_read_b128 v[196:199], v223
	ds_read_b128 v[200:203], v223 offset:1024
	s_setprio 2
	s_lshl_b32 s3, s50, 9
	s_add_i32 s3, s47, s3
	s_add_i32 s3, s3, 0x10380
	s_mov_b32 m0, s43
	v_add_u32_e32 v160, s3, v206
	global_load_lds_dwordx4 v160, s[18:19]
	v_add_u32_e32 v160, s3, v213
	s_mov_b32 m0, s44
	s_nop 0
	global_load_lds_dwordx4 v160, s[18:19]
	s_setprio 0
	s_waitcnt vmcnt(8)
	s_waitcnt lgkmcnt(0)
	s_barrier
	s_waitcnt lgkmcnt(0)
	s_setprio 1
	s_waitcnt lgkmcnt(0)
	v_mfma_f32_16x16x32_f16 v[124:127], v[132:135], v[128:131], v[124:127]
	v_mfma_f32_16x16x32_f16 v[120:123], v[140:143], v[128:131], v[120:123]
	v_mfma_f32_16x16x32_f16 v[116:119], v[132:135], v[152:155], v[116:119]
	v_mfma_f32_16x16x32_f16 v[112:115], v[140:143], v[152:155], v[112:115]
	v_mfma_f32_16x16x32_f16 v[108:111], v[132:135], v[188:191], v[108:111]
	v_mfma_f32_16x16x32_f16 v[104:107], v[140:143], v[188:191], v[104:107]
	v_mfma_f32_16x16x32_f16 v[100:103], v[132:135], v[196:199], v[100:103]
	v_mfma_f32_16x16x32_f16 v[96:99], v[140:143], v[196:199], v[96:99]
	v_mfma_f32_16x16x32_f16 v[160:163], v[136:139], v[148:151], v[124:127]
	v_mfma_f32_16x16x32_f16 v[164:167], v[144:147], v[148:151], v[120:123]
	v_mfma_f32_16x16x32_f16 v[168:171], v[136:139], v[156:159], v[116:119]
	v_mfma_f32_16x16x32_f16 v[172:175], v[144:147], v[156:159], v[112:115]
	v_mfma_f32_16x16x32_f16 v[176:179], v[136:139], v[192:195], v[108:111]
	v_mfma_f32_16x16x32_f16 v[180:183], v[144:147], v[192:195], v[104:107]
	v_mfma_f32_16x16x32_f16 v[100:103], v[136:139], v[200:203], v[100:103]
	v_mfma_f32_16x16x32_f16 v[184:187], v[144:147], v[200:203], v[96:99]
	s_setprio 0
	s_barrier
	ds_read_b128 v[104:107], v219 offset:49152
	ds_read_b128 v[108:111], v219 offset:50176
	ds_read_b128 v[116:119], v219 offset:51200
	ds_read_b128 v[236:239], v219 offset:52224
	s_waitcnt lgkmcnt(0)
	s_barrier
	s_waitcnt lgkmcnt(0)
	s_setprio 1
	s_waitcnt lgkmcnt(0)
	v_mfma_f32_16x16x32_f16 v[52:55], v[104:107], v[128:131], v[52:55]
	v_mfma_f32_16x16x32_f16 v[40:43], v[116:119], v[128:131], v[40:43]
	v_mfma_f32_16x16x32_f16 v[36:39], v[104:107], v[152:155], v[36:39]
	v_mfma_f32_16x16x32_f16 v[32:35], v[116:119], v[152:155], v[32:35]
	v_mfma_f32_16x16x32_f16 v[28:31], v[104:107], v[188:191], v[28:31]
	v_mfma_f32_16x16x32_f16 v[24:27], v[116:119], v[188:191], v[24:27]
	v_mfma_f32_16x16x32_f16 v[20:23], v[104:107], v[196:199], v[20:23]
	v_mfma_f32_16x16x32_f16 v[16:19], v[116:119], v[196:199], v[16:19]
	v_mfma_f32_16x16x32_f16 v[52:55], v[108:111], v[148:151], v[52:55]
	v_mfma_f32_16x16x32_f16 v[40:43], v[236:239], v[148:151], v[40:43]
	v_mfma_f32_16x16x32_f16 v[36:39], v[108:111], v[156:159], v[36:39]
	v_mfma_f32_16x16x32_f16 v[32:35], v[236:239], v[156:159], v[32:35]
	v_mfma_f32_16x16x32_f16 v[28:31], v[108:111], v[192:195], v[28:31]
	v_mfma_f32_16x16x32_f16 v[24:27], v[236:239], v[192:195], v[24:27]
	v_mfma_f32_16x16x32_f16 v[96:99], v[108:111], v[200:203], v[20:23]
	v_mfma_f32_16x16x32_f16 v[16:19], v[236:239], v[200:203], v[16:19]
	s_setprio 0
	s_barrier
	ds_read_b128 v[20:23], v220 offset:16384
	ds_read_b128 v[148:151], v220 offset:17408
	ds_read_b128 v[152:155], v221 offset:16384
	ds_read_b128 v[156:159], v221 offset:17408
	ds_read_b128 v[188:191], v222 offset:16384
	ds_read_b128 v[192:195], v222 offset:17408
	ds_read_b128 v[196:199], v223 offset:16384
	ds_read_b128 v[200:203], v223 offset:17408
	s_waitcnt vmcnt(4)
	s_waitcnt lgkmcnt(0)
	s_barrier
	s_waitcnt lgkmcnt(0)
	s_setprio 1
	s_waitcnt lgkmcnt(0)
	v_mfma_f32_16x16x32_f16 v[0:3], v[140:143], v[152:155], v[0:3]
	v_mfma_f32_16x16x32_f16 v[124:127], v[144:147], v[156:159], v[0:3]
	v_mfma_f32_16x16x32_f16 v[0:3], v[132:135], v[188:191], v[44:47]
	v_mfma_f32_16x16x32_f16 v[128:131], v[136:139], v[192:195], v[0:3]
	v_mfma_f32_16x16x32_f16 v[0:3], v[140:143], v[188:191], v[48:51]
	v_mfma_f32_16x16x32_f16 v[48:51], v[144:147], v[192:195], v[0:3]
	v_mfma_f32_16x16x32_f16 v[0:3], v[132:135], v[196:199], v[56:59]
	v_mfma_f32_16x16x32_f16 v[12:15], v[132:135], v[20:23], v[12:15]
	v_mfma_f32_16x16x32_f16 v[8:11], v[140:143], v[20:23], v[8:11]
	v_mfma_f32_16x16x32_f16 v[4:7], v[132:135], v[152:155], v[4:7]
	v_mfma_f32_16x16x32_f16 v[56:59], v[136:139], v[200:203], v[0:3]
	v_mfma_f32_16x16x32_f16 v[0:3], v[140:143], v[196:199], v[60:63]
	v_mfma_f32_16x16x32_f16 v[112:115], v[136:139], v[148:151], v[12:15]
	v_mfma_f32_16x16x32_f16 v[8:11], v[144:147], v[148:151], v[8:11]
	v_mfma_f32_16x16x32_f16 v[120:123], v[136:139], v[156:159], v[4:7]
	v_mfma_f32_16x16x32_f16 v[60:63], v[144:147], v[200:203], v[0:3]
	s_setprio 0
	s_setprio 1
	v_mfma_f32_16x16x32_f16 v[0:3], v[104:107], v[20:23], v[64:67]
	v_mfma_f32_16x16x32_f16 v[132:135], v[108:111], v[148:151], v[0:3]
	v_mfma_f32_16x16x32_f16 v[0:3], v[116:119], v[20:23], v[68:71]
	v_mfma_f32_16x16x32_f16 v[136:139], v[236:239], v[148:151], v[0:3]
	v_mfma_f32_16x16x32_f16 v[0:3], v[104:107], v[152:155], v[72:75]
	v_mfma_f32_16x16x32_f16 v[140:143], v[108:111], v[156:159], v[0:3]
	v_mfma_f32_16x16x32_f16 v[0:3], v[116:119], v[152:155], v[76:79]
	v_mfma_f32_16x16x32_f16 v[144:147], v[236:239], v[156:159], v[0:3]
	v_mfma_f32_16x16x32_f16 v[0:3], v[104:107], v[188:191], v[80:83]
	v_mfma_f32_16x16x32_f16 v[80:83], v[108:111], v[192:195], v[0:3]
	v_mfma_f32_16x16x32_f16 v[0:3], v[116:119], v[188:191], v[84:87]
	v_mfma_f32_16x16x32_f16 v[148:151], v[236:239], v[192:195], v[0:3]
	v_mfma_f32_16x16x32_f16 v[0:3], v[104:107], v[196:199], v[88:91]
	v_mfma_f32_16x16x32_f16 v[152:155], v[108:111], v[200:203], v[0:3]
	v_mfma_f32_16x16x32_f16 v[0:3], v[116:119], v[196:199], v[92:95]
	v_mfma_f32_16x16x32_f16 v[156:159], v[236:239], v[200:203], v[0:3]
	s_setprio 0
	s_add_i32 s49, s49, s17
	s_cmpk_lt_i32 s49, 0x1c8
	s_cselect_b64 s[6:7], -1, 0
	s_cmpk_gt_i32 s49, 0x1c7
	s_cselect_b64 s[12:13], -1, 0
	s_and_b64 vcc, exec, s[12:13]
	s_mov_b32 s54, s2
	s_mov_b32 s53, s51
	s_mov_b32 s55, s52
	s_barrier
	s_cbranch_vccnz .LBB1_100
	s_cmpk_lt_i32 s49, 0x148
	s_cbranch_scc1 .LBB1_88
	s_cmpk_lt_u32 s49, 0x1a0
	s_cbranch_scc1 .LBB1_89
	s_cmpk_lt_u32 s49, 0x1b8
	s_cbranch_scc1 .LBB1_90
	s_cmpk_lt_u32 s49, 0x1c0
	s_cselect_b32 s47, s45, 0xfffffe40
	s_cselect_b32 s48, 3, 4
	s_mov_b32 s3, 1
	s_cmp_lt_i32 s48, 1
	s_movk_i32 s53, 0x64
	s_cbranch_scc0 .LBB1_91
	s_branch .LBB1_99
